# speedup vs baseline: 1.0348x; 1.0064x over previous
.LBB1_5:
	v_add_u32_e32 v126, s5, v240
	ds_read_b64_tr_b16 v[122:123], v126 offset:24576
	ds_read_b64_tr_b16 v[124:125], v126 offset:25600
	v_mfma_f32_32x32x16_f16 v[98:113], v[206:209], v[146:149], v[2:17]
	v_add_f32_e32 v82, v66, v67
	v_mov_b32_e32 v251, v68
	v_add_f32_e32 v82, v69, v82
	v_add_f32_e32 v251, v70, v251
	v_add_f32_e32 v82, v71, v82
	v_cvt_pk_f16_f32 v162, v66, v67
	v_cvt_pk_f16_f32 v163, v68, v69
	v_add_u32_e32 v128, s5, v239
	ds_read_b64_tr_b16 v[118:119], v128 offset:24576
	ds_read_b64_tr_b16 v[120:121], v128 offset:25600
	v_add_f32_e32 v66, v72, v82
	v_mfma_f32_32x32x16_f16 v[82:97], v[202:205], v[146:149], v[2:17]
	v_add_f32_e32 v251, v73, v251
	v_add_f32_e32 v66, v74, v66
	v_add_f32_e32 v251, v75, v251
	v_cvt_pk_f16_f32 v164, v70, v71
	v_cvt_pk_f16_f32 v165, v72, v73
	ds_read_b64_tr_b16 v[114:115], v126 offset:26624
	ds_read_b64_tr_b16 v[116:117], v126 offset:27648
	v_mfma_f32_32x32x16_f16 v[98:113], v[198:201], v[150:153], v[98:113]
	v_add_f32_e32 v66, v76, v66
	v_add_f32_e32 v251, v77, v251
	v_add_f32_e32 v66, v78, v66
	v_add_f32_e32 v251, v79, v251
	v_cvt_pk_f16_f32 v166, v74, v75
	v_cvt_pk_f16_f32 v167, v76, v77
	ds_read_b64_tr_b16 v[70:71], v128 offset:26624
	ds_read_b64_tr_b16 v[72:73], v128 offset:27648
	v_mfma_f32_32x32x16_f16 v[82:97], v[194:197], v[150:153], v[82:97]
	v_add_f32_e32 v66, v80, v66
	v_add_f32_e32 v251, v81, v251
	v_add_f32_e32 v66, v50, v66
	v_add_f32_e32 v74, v51, v66
	v_cvt_pk_f16_f32 v168, v78, v79
	v_cvt_pk_f16_f32 v169, v80, v81
	ds_read_b64_tr_b16 v[66:67], v126 offset:28672
	ds_read_b64_tr_b16 v[68:69], v126 offset:29696
	v_mfma_f32_32x32x16_f16 v[98:113], v[190:193], v[154:157], v[98:113]
	v_add_f32_e32 v251, v52, v251
	v_add_f32_e32 v74, v53, v74
	v_add_f32_e32 v251, v54, v251
	v_add_f32_e32 v74, v55, v74
	v_cvt_pk_f16_f32 v170, v50, v51
	v_cvt_pk_f16_f32 v171, v52, v53
	ds_read_b64_tr_b16 v[50:51], v128 offset:28672
	ds_read_b64_tr_b16 v[52:53], v128 offset:29696
	v_mfma_f32_32x32x16_f16 v[82:97], v[186:189], v[154:157], v[82:97]
	v_add_f32_e32 v251, v56, v251
	v_add_f32_e32 v74, v57, v74
	v_add_f32_e32 v251, v58, v251
	v_add_f32_e32 v74, v59, v74
	v_cvt_pk_f16_f32 v172, v54, v55
	v_cvt_pk_f16_f32 v173, v56, v57
	ds_read_b64_tr_b16 v[54:55], v126 offset:30720
	ds_read_b64_tr_b16 v[56:57], v126 offset:31744
	v_mfma_f32_32x32x16_f16 v[98:113], v[182:185], v[158:161], v[98:113]
	v_add_f32_e32 v251, v60, v251
	v_add_f32_e32 v74, v61, v74
	v_add_f32_e32 v251, v62, v251
	v_add_f32_e32 v74, v63, v74
	v_cvt_pk_f16_f32 v174, v58, v59
	v_cvt_pk_f16_f32 v175, v60, v61
	ds_read_b64_tr_b16 v[58:59], v128 offset:30720
	ds_read_b64_tr_b16 v[60:61], v128 offset:31744
	v_mfma_f32_32x32x16_f16 v[82:97], v[178:181], v[158:161], v[82:97]
	v_add_f32_e32 v251, v64, v251
	v_add_f32_e32 v74, v65, v74
	v_add_f32_e32 v74, v251, v74
	v_cvt_pk_f16_f32 v176, v62, v63
	v_cvt_pk_f16_f32 v177, v64, v65
	v_max_f32_e32 v62, v99, v98
	v_max3_f32 v63, v100, v101, v102
	v_max3_f32 v62, v62, v103, v104
	v_max3_f32 v63, v63, v105, v106
	v_max3_f32 v62, v62, v107, v108
	v_max3_f32 v63, v63, v109, v110
	v_max3_f32 v62, v62, v111, v112
	v_max3_f32 v63, v63, v113, v82
	v_max3_f32 v62, v62, v83, v84
	v_max3_f32 v63, v63, v85, v86
	v_max3_f32 v62, v62, v87, v88
	v_max3_f32 v63, v63, v89, v90
	v_max3_f32 v62, v62, v91, v92
	v_max3_f32 v63, v63, v93, v94
	v_max3_f32 v62, v62, v95, v96
	v_max3_f32 v62, v62, v97, v63
	v_mov_b32_e32 v63, v62
	s_nop 1
	v_permlane32_swap_b32_e32 v62, v63
	v_max_f32_e32 v62, v63, v62
	v_cmp_lt_f32_e32 vcc, s34, v62
	s_cmp_lg_u64 vcc, 0
	v_add_f32_e32 v182, v127, v74
	s_cselect_b64 s[8:9], -1, 0
	s_cbranch_vccnz .LBB1_25
.LBB1_6:
	s_waitcnt lgkmcnt(0)
	v_mfma_f32_32x32x16_f16 v[34:49], v[162:165], v[122:125], v[34:49]
	v_exp_f32_e32 v98, v98
	v_exp_f32_e32 v99, v99
	v_exp_f32_e32 v100, v100
	v_exp_f32_e32 v101, v101
	s_sub_i32 s43, s38, s27
	s_add_i32 s43, s43, 34
	s_add_i32 s44, s18, -1
	s_cmp_ge_i32 s44, s28
	s_cselect_b32 s45, s28, 0
	s_sub_i32 s44, s44, s45
	s_and_b64 s[48:49], s[6:7], exec
	s_cselect_b32 s43, s44, s43
	v_mad_i64_i32 v[252:253], s[50:51], s43, v244, v[222:223]
	s_add_i32 s44, s38, 1
	s_cmp_ge_i32 s44, s29
	s_cselect_b32 s44, s29, 0
	s_sub_i32 s44, 0, s44
	s_and_b64 s[48:49], s[6:7], exec
	s_cselect_b32 s44, s44, s28
	s_add_i32 s44, s44, s18
	s_add_i32 s44, s44, -3
	v_mad_i64_i32 v[254:255], s[50:51], s44, v244, v[224:225]
	s_add_i32 s52, s35, s30
	s_add_i32 s53, s36, s31
	v_mfma_f32_32x32x16_f16 v[18:33], v[162:165], v[118:121], v[18:33]
	v_exp_f32_e32 v102, v102
	v_exp_f32_e32 v103, v103
	v_exp_f32_e32 v104, v104
	v_exp_f32_e32 v105, v105
	v_add_u32_e32 v74, s36, v234
	ds_read_b128 v[62:65], v74
	ds_read_b128 v[138:141], v74 offset:4096
	v_mfma_f32_32x32x16_f16 v[34:49], v[166:169], v[114:117], v[34:49]
	v_exp_f32_e32 v106, v106
	v_exp_f32_e32 v107, v107
	v_exp_f32_e32 v108, v108
	v_exp_f32_e32 v109, v109
	v_add_u32_e32 v74, s36, v235
	ds_read_b128 v[178:181], v74
	ds_read_b128 v[126:129], v74 offset:4096
	v_mfma_f32_32x32x16_f16 v[18:33], v[166:169], v[70:73], v[18:33]
	v_exp_f32_e32 v110, v110
	v_exp_f32_e32 v111, v111
	v_exp_f32_e32 v112, v112
	v_exp_f32_e32 v113, v113
	v_add_u32_e32 v70, s36, v236
	ds_read_b128 v[130:133], v70
	ds_read_b128 v[118:121], v70 offset:4096
	v_mfma_f32_32x32x16_f16 v[34:49], v[170:173], v[66:69], v[34:49]
	v_exp_f32_e32 v82, v82
	v_exp_f32_e32 v83, v83
	v_exp_f32_e32 v84, v84
	v_exp_f32_e32 v85, v85
	v_add_u32_e32 v66, s36, v237
	ds_read_b128 v[122:125], v66
	ds_read_b128 v[114:117], v66 offset:4096
	v_mfma_f32_32x32x16_f16 v[18:33], v[170:173], v[50:53], v[18:33]
	v_exp_f32_e32 v86, v86
	v_exp_f32_e32 v87, v87
	v_exp_f32_e32 v88, v88
	v_exp_f32_e32 v89, v89
	v_mfma_f32_32x32x16_f16 v[34:49], v[174:177], v[54:57], v[34:49]
	v_exp_f32_e32 v90, v90
	v_exp_f32_e32 v91, v91
	v_exp_f32_e32 v92, v92
	v_exp_f32_e32 v93, v93
	v_mfma_f32_32x32x16_f16 v[18:33], v[174:177], v[58:61], v[18:33]
	v_exp_f32_e32 v94, v94
	v_exp_f32_e32 v95, v95
	v_exp_f32_e32 v96, v96
	v_exp_f32_e32 v97, v97
	s_mov_b32 m0, s52
	s_addk_i32 s52, 0x1000
	global_load_lds_dwordx4 v[252:253], off
	s_mov_b32 m0, s52
	v_lshl_add_u64 v[252:253], v[252:253], 0, s[10:11]
	global_load_lds_dwordx4 v[252:253], off
	s_mov_b32 m0, s53
	s_addk_i32 s53, 0x1000
	global_load_lds_dwordx4 v[254:255], off
	s_mov_b32 m0, s53
	v_lshl_add_u64 v[254:255], v[254:255], 0, s[10:11]
	global_load_lds_dwordx4 v[254:255], off
	s_waitcnt vmcnt(4) lgkmcnt(0)
	s_barrier
	s_andn2_b64 vcc, exec, s[8:9]
	s_cbranch_vccnz .LBB1_12
	v_add_u32_e32 v66, s24, v233
	ds_read_b128 v[50:53], v66 offset:96
	ds_read_b128 v[54:57], v66 offset:64
	ds_read_b128 v[58:61], v66 offset:32
	ds_read_b128 v[66:69], v66
	s_waitcnt lgkmcnt(3)
	v_pk_mul_f32 v[46:47], v[46:47], v[50:51]
	s_waitcnt lgkmcnt(2)
	v_pk_mul_f32 v[42:43], v[42:43], v[54:55]
	s_waitcnt lgkmcnt(1)
	v_pk_mul_f32 v[38:39], v[38:39], v[58:59]
	v_pk_mul_f32 v[48:49], v[48:49], v[52:53]
	v_pk_mul_f32 v[44:45], v[44:45], v[56:57]
	v_pk_mul_f32 v[40:41], v[40:41], v[60:61]
	s_waitcnt lgkmcnt(0)
	v_pk_mul_f32 v[36:37], v[36:37], v[68:69]
	v_pk_mul_f32 v[34:35], v[34:35], v[66:67]
	v_pk_mul_f32 v[30:31], v[30:31], v[50:51]
	v_pk_mul_f32 v[26:27], v[26:27], v[54:55]
	v_pk_mul_f32 v[22:23], v[22:23], v[58:59]
	v_pk_mul_f32 v[32:33], v[32:33], v[52:53]
	v_pk_mul_f32 v[28:29], v[28:29], v[56:57]
	v_pk_mul_f32 v[24:25], v[24:25], v[60:61]
	v_pk_mul_f32 v[20:21], v[20:21], v[68:69]
	v_pk_mul_f32 v[18:19], v[18:19], v[66:67]
.LBB1_12:
	v_add_u32_e32 v174, s35, v240
	ds_read_b64_tr_b16 v[134:135], v174 offset:24576
	ds_read_b64_tr_b16 v[136:137], v174 offset:25600
	v_mfma_f32_32x32x16_f16 v[66:81], v[62:65], v[146:149], v[2:17]
	v_add_f32_e32 v50, v98, v99
	v_mov_b32_e32 v251, v100
	v_add_f32_e32 v50, v101, v50
	v_add_f32_e32 v251, v102, v251
	v_add_f32_e32 v50, v103, v50
	v_cvt_pk_f16_f32 v162, v98, v99
	v_cvt_pk_f16_f32 v163, v100, v101
	v_add_u32_e32 v183, s35, v239
	ds_read_b64_tr_b16 v[142:143], v183 offset:24576
	ds_read_b64_tr_b16 v[144:145], v183 offset:25600
	v_add_f32_e32 v251, v104, v251
	v_add_f32_e32 v50, v105, v50
	v_add_f32_e32 v251, v106, v251
	v_add_f32_e32 v98, v107, v50
	v_mfma_f32_32x32x16_f16 v[50:65], v[138:141], v[146:149], v[2:17]
	v_cvt_pk_f16_f32 v164, v102, v103
	v_cvt_pk_f16_f32 v165, v104, v105
	ds_read_b64_tr_b16 v[138:139], v174 offset:26624
	ds_read_b64_tr_b16 v[140:141], v174 offset:27648
	v_mfma_f32_32x32x16_f16 v[66:81], v[178:181], v[150:153], v[66:81]
	v_add_f32_e32 v251, v108, v251
	v_add_f32_e32 v98, v109, v98
	v_add_f32_e32 v251, v110, v251
	v_add_f32_e32 v98, v111, v98
	v_cvt_pk_f16_f32 v166, v106, v107
	v_cvt_pk_f16_f32 v167, v108, v109
	ds_read_b64_tr_b16 v[102:103], v183 offset:26624
	ds_read_b64_tr_b16 v[104:105], v183 offset:27648
	v_mfma_f32_32x32x16_f16 v[50:65], v[126:129], v[150:153], v[50:65]
	v_add_f32_e32 v251, v112, v251
	v_add_f32_e32 v98, v113, v98
	v_add_f32_e32 v251, v82, v251
	v_add_f32_e32 v106, v83, v98
	v_cvt_pk_f16_f32 v168, v110, v111
	v_cvt_pk_f16_f32 v169, v112, v113
	ds_read_b64_tr_b16 v[98:99], v174 offset:28672
	ds_read_b64_tr_b16 v[100:101], v174 offset:29696
	v_mfma_f32_32x32x16_f16 v[66:81], v[130:133], v[154:157], v[66:81]
	v_add_f32_e32 v251, v84, v251
	v_add_f32_e32 v106, v85, v106
	v_add_f32_e32 v251, v86, v251
	v_add_f32_e32 v106, v87, v106
	v_cvt_pk_f16_f32 v170, v82, v83
	v_cvt_pk_f16_f32 v171, v84, v85
	ds_read_b64_tr_b16 v[82:83], v183 offset:28672
	ds_read_b64_tr_b16 v[84:85], v183 offset:29696
	v_mfma_f32_32x32x16_f16 v[50:65], v[118:121], v[154:157], v[50:65]
	v_add_f32_e32 v251, v88, v251
	v_add_f32_e32 v106, v89, v106
	v_add_f32_e32 v251, v90, v251
	v_add_f32_e32 v106, v91, v106
	v_cvt_pk_f16_f32 v172, v86, v87
	v_cvt_pk_f16_f32 v173, v88, v89
	ds_read_b64_tr_b16 v[86:87], v174 offset:30720
	ds_read_b64_tr_b16 v[88:89], v174 offset:31744
	v_mfma_f32_32x32x16_f16 v[66:81], v[122:125], v[158:161], v[66:81]
	v_add_f32_e32 v251, v92, v251
	v_add_f32_e32 v106, v93, v106
	v_add_f32_e32 v251, v94, v251
	v_add_f32_e32 v106, v95, v106
	v_cvt_pk_f16_f32 v174, v90, v91
	v_cvt_pk_f16_f32 v175, v92, v93
	ds_read_b64_tr_b16 v[90:91], v183 offset:30720
	ds_read_b64_tr_b16 v[92:93], v183 offset:31744
	v_mfma_f32_32x32x16_f16 v[50:65], v[114:117], v[158:161], v[50:65]
	v_add_f32_e32 v251, v96, v251
	v_add_f32_e32 v106, v97, v106
	v_add_f32_e32 v106, v251, v106
	v_cvt_pk_f16_f32 v176, v94, v95
	v_cvt_pk_f16_f32 v177, v96, v97
	v_max_f32_e32 v94, v67, v66
	v_max3_f32 v95, v68, v69, v70
	v_max3_f32 v94, v94, v71, v72
	v_max3_f32 v95, v95, v73, v74
	v_max3_f32 v94, v94, v75, v76
	v_max3_f32 v95, v95, v77, v78
	v_max3_f32 v94, v94, v79, v80
	v_max3_f32 v95, v95, v81, v50
	v_max3_f32 v94, v94, v51, v52
	v_max3_f32 v95, v95, v53, v54
	v_max3_f32 v94, v94, v55, v56
	v_max3_f32 v95, v95, v57, v58
	v_max3_f32 v94, v94, v59, v60
	v_max3_f32 v95, v95, v61, v62
	v_max3_f32 v94, v94, v63, v64
	v_max3_f32 v94, v94, v65, v95
	v_mov_b32_e32 v95, v94
	s_nop 1
	v_permlane32_swap_b32_e32 v94, v95
	v_max_f32_e32 v94, v95, v94
	v_cmp_lt_f32_e32 vcc, s34, v94
	s_cmp_lg_u64 vcc, 0
	v_add_f32_e32 v127, v182, v106
	s_cselect_b64 s[8:9], -1, 0
	s_cbranch_vccnz .LBB1_28
.LBB1_13:
	s_add_i32 s16, s36, 0x2000
	s_cmpk_lg_i32 s36, 0x4000
	s_cselect_b32 s35, s16, 0
	s_waitcnt lgkmcnt(0)
	v_mfma_f32_32x32x16_f16 v[34:49], v[162:165], v[134:137], v[34:49]
	v_exp_f32_e32 v66, v66
	v_exp_f32_e32 v67, v67
	v_exp_f32_e32 v68, v68
	v_exp_f32_e32 v69, v69
	s_sub_i32 s43, s38, s27
	s_add_i32 s45, s43, 33
	s_add_i32 s43, s43, 35
	s_cmp_ge_i32 s18, s28
	s_cselect_b32 s44, s28, 0
	s_sub_i32 s44, s18, s44
	s_and_b64 s[48:49], s[6:7], exec
	s_cselect_b32 s43, s44, s43
	v_mad_i64_i32 v[252:253], s[50:51], s43, v244, v[222:223]
	s_add_i32 s44, s18, -2
	s_cmp_ge_i32 s44, s28
	s_cselect_b32 s46, s28, 0
	s_sub_i32 s44, s44, s46
	s_and_b64 s[48:49], s[6:7], exec
	s_cselect_b32 s44, s44, s45
	v_mad_i64_i32 v[254:255], s[50:51], s44, v244, v[224:225]
	s_add_i32 s52, s36, s30
	s_add_i32 s53, s35, s31
	s_add_i32 s46, s35, 0x2000
	s_cmpk_lg_i32 s35, 0x4000
	s_cselect_b32 s37, s46, 0
	s_add_i32 s39, s18, -2
	v_mfma_f32_32x32x16_f16 v[18:33], v[162:165], v[142:145], v[18:33]
	v_exp_f32_e32 v70, v70
	v_exp_f32_e32 v71, v71
	v_exp_f32_e32 v72, v72
	v_exp_f32_e32 v73, v73
	v_add_u32_e32 v94, s35, v234
	ds_read_b128 v[206:209], v94
	ds_read_b128 v[202:205], v94 offset:4096
	v_mfma_f32_32x32x16_f16 v[34:49], v[166:169], v[138:141], v[34:49]
	v_exp_f32_e32 v74, v74
	v_exp_f32_e32 v75, v75
	v_exp_f32_e32 v76, v76
	v_exp_f32_e32 v77, v77
	v_add_u32_e32 v94, s35, v235
	ds_read_b128 v[198:201], v94
	ds_read_b128 v[194:197], v94 offset:4096
	v_mfma_f32_32x32x16_f16 v[18:33], v[166:169], v[102:105], v[18:33]
	v_exp_f32_e32 v78, v78
	v_exp_f32_e32 v79, v79
	v_exp_f32_e32 v80, v80
	v_exp_f32_e32 v81, v81
	v_add_u32_e32 v94, s35, v236
	ds_read_b128 v[190:193], v94
	ds_read_b128 v[186:189], v94 offset:4096
	v_mfma_f32_32x32x16_f16 v[34:49], v[170:173], v[98:101], v[34:49]
	v_exp_f32_e32 v50, v50
	v_exp_f32_e32 v51, v51
	v_exp_f32_e32 v52, v52
	v_exp_f32_e32 v53, v53
	v_add_u32_e32 v94, s35, v237
	ds_read_b128 v[182:185], v94
	ds_read_b128 v[178:181], v94 offset:4096
	v_mfma_f32_32x32x16_f16 v[18:33], v[170:173], v[82:85], v[18:33]
	v_exp_f32_e32 v54, v54
	v_exp_f32_e32 v55, v55
	v_exp_f32_e32 v56, v56
	v_exp_f32_e32 v57, v57
	v_mfma_f32_32x32x16_f16 v[34:49], v[174:177], v[86:89], v[34:49]
	v_exp_f32_e32 v58, v58
	v_exp_f32_e32 v59, v59
	v_exp_f32_e32 v60, v60
	v_exp_f32_e32 v61, v61
	v_mfma_f32_32x32x16_f16 v[18:33], v[174:177], v[90:93], v[18:33]
	v_exp_f32_e32 v62, v62
	v_exp_f32_e32 v63, v63
	v_exp_f32_e32 v64, v64
	v_exp_f32_e32 v65, v65
	s_mov_b32 m0, s52
	s_addk_i32 s52, 0x1000
	global_load_lds_dwordx4 v[252:253], off
	s_mov_b32 m0, s52
	v_lshl_add_u64 v[252:253], v[252:253], 0, s[10:11]
	global_load_lds_dwordx4 v[252:253], off
	s_mov_b32 m0, s53
	s_addk_i32 s53, 0x1000
	global_load_lds_dwordx4 v[254:255], off
	s_mov_b32 m0, s53
	v_lshl_add_u64 v[254:255], v[254:255], 0, s[10:11]
	global_load_lds_dwordx4 v[254:255], off
	s_waitcnt vmcnt(4) lgkmcnt(0)
	s_barrier
	s_andn2_b64 vcc, exec, s[8:9]
	s_cbranch_vccnz .LBB1_23
	v_add_u32_e32 v94, s24, v233
	ds_read_b128 v[82:85], v94 offset:96
	ds_read_b128 v[86:89], v94 offset:64
	ds_read_b128 v[90:93], v94
	ds_read_b128 v[94:97], v94 offset:32
	s_waitcnt lgkmcnt(3)
	v_pk_mul_f32 v[48:49], v[48:49], v[84:85]
	v_pk_mul_f32 v[46:47], v[46:47], v[82:83]
	s_waitcnt lgkmcnt(2)
	v_pk_mul_f32 v[44:45], v[44:45], v[88:89]
	v_pk_mul_f32 v[42:43], v[42:43], v[86:87]
	s_waitcnt lgkmcnt(0)
	v_pk_mul_f32 v[40:41], v[40:41], v[96:97]
	v_pk_mul_f32 v[38:39], v[38:39], v[94:95]
	v_pk_mul_f32 v[36:37], v[36:37], v[92:93]
	v_pk_mul_f32 v[34:35], v[34:35], v[90:91]
	v_pk_mul_f32 v[32:33], v[32:33], v[84:85]
	v_pk_mul_f32 v[30:31], v[30:31], v[82:83]
	v_pk_mul_f32 v[28:29], v[28:29], v[88:89]
	v_pk_mul_f32 v[26:27], v[26:27], v[86:87]
	v_pk_mul_f32 v[24:25], v[24:25], v[96:97]
	v_pk_mul_f32 v[22:23], v[22:23], v[94:95]
	v_pk_mul_f32 v[20:21], v[20:21], v[92:93]
	v_pk_mul_f32 v[18:19], v[18:19], v[90:91]
